# speedup vs baseline: 1.0122x; 1.0017x over previous
.LBB1_3:
	s_mov_b32 s29, s16
	v_add_u32_e32 v0, s29, v101
	ds_read_b128 v[94:97], v0 offset:16384
	ds_read_b128 v[102:105], v0 offset:17408
	ds_read_b128 v[106:109], v0 offset:18432
	ds_read_b128 v[110:113], v0 offset:19456
	ds_read_b128 v[114:117], v0 offset:32768
	ds_read_b128 v[118:121], v0 offset:33792
	ds_read_b128 v[122:125], v0 offset:34816
	ds_read_b128 v[126:129], v0 offset:35840
	v_add_u32_e32 v0, s29, v91
	ds_read_b128 v[130:133], v0
	ds_read_b128 v[134:137], v0 offset:1024
	ds_read_b128 v[138:141], v0 offset:2048
	ds_read_b128 v[142:145], v0 offset:3072
	ds_read_b128 v[146:149], v0 offset:4096
	ds_read_b128 v[150:153], v0 offset:5120
	ds_read_b128 v[154:157], v0 offset:6144
	ds_read_b128 v[158:161], v0 offset:7168
	s_lshl_b32 s16, s28, 2
	s_or_b32 s16, s16, s23
	s_lshl_b64 s[30:31], s[16:17], 19
	s_add_u32 s16, s6, s30
	s_addc_u32 s31, s7, s31
	s_lshl_b32 s33, s3, 7
	s_ashr_i32 s35, s33, 31
	s_add_u32 s30, s16, s33
	s_addc_u32 s31, s31, s35
	s_add_u32 s34, s4, s33
	s_addc_u32 s35, s5, s35
	s_add_i32 s16, s19, s27
	s_add_i32 m0, s16, 0x4000
	s_nop 0
	global_load_lds_dwordx4 v84, s[30:31]
	s_add_i32 m0, s16, 0x6000
	s_nop 0
	global_load_lds_dwordx4 v88, s[30:31]
	s_mov_b32 m0, s16
	s_nop 0
	global_load_lds_dwordx4 v82, s[34:35]
	s_waitcnt vmcnt(3)
	s_waitcnt lgkmcnt(0)
	s_barrier
	s_setprio 1
	s_waitcnt lgkmcnt(0)
	v_mfma_f32_16x16x32_f16 v[78:81], v[94:97], v[130:133], v[78:81]
	s_add_u32 s30, s30, 0x40000
	s_addc_u32 s31, s31, 0
	s_add_i32 m0, s16, 0x8000
	v_mfma_f32_16x16x32_f16 v[74:77], v[106:109], v[130:133], v[74:77]
	global_load_lds_dwordx4 v84, s[30:31]
	s_add_i32 m0, s16, 0xa000
	v_mfma_f32_16x16x32_f16 v[66:69], v[94:97], v[138:141], v[66:69]
	global_load_lds_dwordx4 v88, s[30:31]
	s_add_i32 m0, s16, 0x2000
	v_mfma_f32_16x16x32_f16 v[58:61], v[106:109], v[138:141], v[58:61]
	global_load_lds_dwordx4 v86, s[34:35]
	v_mfma_f32_16x16x32_f16 v[78:81], v[102:105], v[134:137], v[78:81]
	v_mfma_f32_16x16x32_f16 v[74:77], v[110:113], v[134:137], v[74:77]
	v_mfma_f32_16x16x32_f16 v[66:69], v[102:105], v[142:145], v[66:69]
	v_mfma_f32_16x16x32_f16 v[58:61], v[110:113], v[142:145], v[58:61]
	v_mfma_f32_16x16x32_f16 v[54:57], v[94:97], v[146:149], v[54:57]
	v_mfma_f32_16x16x32_f16 v[46:49], v[106:109], v[146:149], v[46:49]
	v_mfma_f32_16x16x32_f16 v[34:37], v[94:97], v[154:157], v[34:37]
	v_mfma_f32_16x16x32_f16 v[26:29], v[106:109], v[154:157], v[26:29]
	v_mfma_f32_16x16x32_f16 v[54:57], v[102:105], v[150:153], v[54:57]
	v_mfma_f32_16x16x32_f16 v[46:49], v[110:113], v[150:153], v[46:49]
	v_mfma_f32_16x16x32_f16 v[34:37], v[102:105], v[158:161], v[34:37]
	v_mfma_f32_16x16x32_f16 v[26:29], v[110:113], v[158:161], v[26:29]
	v_mfma_f32_16x16x32_f16 v[70:73], v[114:117], v[130:133], v[70:73]
	v_mfma_f32_16x16x32_f16 v[62:65], v[122:125], v[130:133], v[62:65]
	v_mfma_f32_16x16x32_f16 v[50:53], v[114:117], v[138:141], v[50:53]
	v_mfma_f32_16x16x32_f16 v[42:45], v[122:125], v[138:141], v[42:45]
	v_mfma_f32_16x16x32_f16 v[70:73], v[118:121], v[134:137], v[70:73]
	v_mfma_f32_16x16x32_f16 v[62:65], v[126:129], v[134:137], v[62:65]
	v_mfma_f32_16x16x32_f16 v[50:53], v[118:121], v[142:145], v[50:53]
	v_mfma_f32_16x16x32_f16 v[42:45], v[126:129], v[142:145], v[42:45]
	v_mfma_f32_16x16x32_f16 v[38:41], v[114:117], v[146:149], v[38:41]
	v_mfma_f32_16x16x32_f16 v[30:33], v[122:125], v[146:149], v[30:33]
	s_add_i32 s3, s3, 1
	s_bitcmp1_b32 s3, 4
	s_addc_u32 s28, s28, 0
	v_mfma_f32_16x16x32_f16 v[22:25], v[114:117], v[154:157], v[22:25]
	s_and_b32 s3, s3, 15
	v_mfma_f32_16x16x32_f16 v[2:5], v[122:125], v[154:157], v[2:5]
	v_mfma_f32_16x16x32_f16 v[38:41], v[118:121], v[150:153], v[38:41]
	v_mfma_f32_16x16x32_f16 v[30:33], v[126:129], v[150:153], v[30:33]
	s_add_i32 s26, s26, -1
	v_mfma_f32_16x16x32_f16 v[22:25], v[118:121], v[158:161], v[22:25]
	s_mov_b32 s16, s24
	s_mov_b32 s24, s27
	v_mfma_f32_16x16x32_f16 v[2:5], v[126:129], v[158:161], v[2:5]
	s_mov_b32 s27, s29
	s_cmp_lg_u32 s26, 0
	s_setprio 0
	s_barrier
	s_cbranch_scc1 .LBB1_3
	s_lshl_b32 s3, s14, 7
	s_add_i32 s17, s25, s3
	s_ashr_i32 s3, s17, 1
	s_lshr_b32 s14, s17, 5
	s_or_b32 s24, s15, s2
	s_and_b32 s14, s14, 62
	s_and_b32 s27, s3, 0xfffffc00
	v_or_b32_e32 v105, s24, v1
	v_lshlrev_b32_e32 v98, 4, v93
	v_or_b32_e32 v102, 16, v93
	v_or_b32_e32 v103, 32, v93
	v_or_b32_e32 v104, 48, v93
	v_mov_b32_e32 v93, 0
	s_and_b32 s16, s24, 0x340
	v_lshlrev_b32_e32 v95, 6, v105
	s_or_b32 s2, s27, s14
	v_lshlrev_b32_e32 v0, 9, v92
	v_and_b32_e32 v110, 0xc00, v95
	v_mov_b32_e32 v111, v93
	s_or_b32 s14, s2, s16
	v_and_b32_e32 v92, 0x200, v0
	v_lshl_add_u64 v[110:111], s[8:9], 0, v[110:111]
	s_or_b32 s30, s14, 0x80
	s_mov_b32 s3, 0
	v_mov_b32_e32 v99, v93
	v_lshl_add_u64 v[110:111], v[110:111], 0, v[92:93]
	s_mov_b32 s2, 0x3e38aa3b
	v_pk_add_f32 v[72:73], v[12:13], v[72:73]
	v_pk_add_f32 v[70:71], v[10:11], v[70:71]
	v_pk_add_f32 v[64:65], v[8:9], v[64:65]
	v_pk_add_f32 v[62:63], v[6:7], v[62:63]
	s_ashr_i32 s31, s30, 31
	v_lshl_add_u64 v[112:113], v[110:111], 0, v[98:99]
	v_pk_mul_f32 v[72:73], v[72:73], s[2:3] op_sel_hi:[1,0]
	v_pk_mul_f32 v[70:71], v[70:71], s[2:3] op_sel_hi:[1,0]
	v_pk_mul_f32 v[64:65], v[64:65], s[2:3] op_sel_hi:[1,0]
	v_pk_mul_f32 v[62:63], v[62:63], s[2:3] op_sel_hi:[1,0]
	s_lshl_b64 s[30:31], s[30:31], 12
	v_lshlrev_b32_e32 v96, 4, v102
	v_mov_b32_e32 v97, v93
	v_pk_add_f32 v[80:81], v[20:21], v[80:81]
	v_pk_add_f32 v[78:79], v[18:19], v[78:79]
	v_pk_add_f32 v[74:75], v[14:15], v[74:75]
	s_ashr_i32 s15, s14, 31
	v_cvt_pk_f16_f32 v70, v70, v71
	v_cvt_pk_f16_f32 v71, v72, v73
	v_cvt_pk_f16_f32 v72, v62, v63
	v_cvt_pk_f16_f32 v73, v64, v65
	v_lshl_add_u64 v[62:63], v[112:113], 0, s[30:31]
	v_pk_add_f32 v[58:59], v[14:15], v[58:59]
	v_pk_mul_f32 v[80:81], v[80:81], s[2:3] op_sel_hi:[1,0]
	v_pk_mul_f32 v[78:79], v[78:79], s[2:3] op_sel_hi:[1,0]
	v_pk_mul_f32 v[74:75], v[74:75], s[2:3] op_sel_hi:[1,0]
	s_lshl_b64 s[28:29], s[14:15], 12
	global_store_dwordx4 v[62:63], v[70:73], off
	v_pk_add_f32 v[62:63], v[20:21], v[68:69]
	v_pk_add_f32 v[64:65], v[18:19], v[66:67]
	v_lshl_add_u64 v[70:71], v[110:111], 0, v[96:97]
	v_pk_mul_f32 v[58:59], v[58:59], s[2:3] op_sel_hi:[1,0]
	v_pk_add_f32 v[52:53], v[12:13], v[52:53]
	v_pk_add_f32 v[50:51], v[10:11], v[50:51]
	v_pk_add_f32 v[44:45], v[8:9], v[44:45]
	v_pk_add_f32 v[42:43], v[6:7], v[42:43]
	v_lshlrev_b32_e32 v0, 4, v103
	v_cvt_pk_f16_f32 v78, v78, v79
	v_cvt_pk_f16_f32 v79, v80, v81
	v_cvt_pk_f16_f32 v80, v74, v75
	v_lshl_add_u64 v[74:75], v[112:113], 0, s[28:29]
	v_pk_mul_f32 v[66:67], v[62:63], s[2:3] op_sel_hi:[1,0]
	v_pk_mul_f32 v[62:63], v[64:65], s[2:3] op_sel_hi:[1,0]
	v_cvt_pk_f16_f32 v64, v58, v59
	v_lshl_add_u64 v[58:59], v[70:71], 0, s[28:29]
	v_pk_mul_f32 v[52:53], v[52:53], s[2:3] op_sel_hi:[1,0]
	v_pk_mul_f32 v[50:51], v[50:51], s[2:3] op_sel_hi:[1,0]
	v_pk_mul_f32 v[44:45], v[44:45], s[2:3] op_sel_hi:[1,0]
	v_pk_mul_f32 v[42:43], v[42:43], s[2:3] op_sel_hi:[1,0]
	s_or_b32 s28, s14, 1
	s_or_b32 s14, s14, 0x81
	v_and_b32_e32 v106, 0xf0, v0
	v_mov_b32_e32 v107, v93
	v_cvt_pk_f16_f32 v50, v50, v51
	v_cvt_pk_f16_f32 v51, v52, v53
	v_cvt_pk_f16_f32 v52, v42, v43
	v_cvt_pk_f16_f32 v53, v44, v45
	v_lshl_add_u64 v[42:43], v[70:71], 0, s[30:31]
	v_pk_add_f32 v[40:41], v[12:13], v[40:41]
	v_pk_add_f32 v[38:39], v[10:11], v[38:39]
	v_pk_add_f32 v[32:33], v[8:9], v[32:33]
	v_pk_add_f32 v[30:31], v[6:7], v[30:31]
	s_ashr_i32 s15, s14, 31
	v_lshlrev_b32_e32 v94, 4, v104
	global_store_dwordx4 v[42:43], v[50:53], off
	v_pk_mul_f32 v[40:41], v[40:41], s[2:3] op_sel_hi:[1,0]
	v_pk_mul_f32 v[38:39], v[38:39], s[2:3] op_sel_hi:[1,0]
	v_lshl_add_u64 v[50:51], v[110:111], 0, v[106:107]
	v_pk_mul_f32 v[32:33], v[32:33], s[2:3] op_sel_hi:[1,0]
	v_pk_mul_f32 v[30:31], v[30:31], s[2:3] op_sel_hi:[1,0]
	s_lshl_b64 s[14:15], s[14:15], 12
	v_and_b32_e32 v108, 0x1f0, v94
	v_mov_b32_e32 v109, v93
	v_pk_add_f32 v[42:43], v[20:21], v[56:57]
	v_pk_add_f32 v[44:45], v[18:19], v[54:55]
	v_pk_add_f32 v[46:47], v[14:15], v[46:47]
	s_ashr_i32 s29, s28, 31
	v_cvt_pk_f16_f32 v38, v38, v39
	v_cvt_pk_f16_f32 v39, v40, v41
	v_cvt_pk_f16_f32 v40, v30, v31
	v_cvt_pk_f16_f32 v41, v32, v33
	v_lshl_add_u64 v[30:31], v[50:51], 0, s[14:15]
	v_pk_add_f32 v[20:21], v[20:21], v[36:37]
	v_pk_add_f32 v[18:19], v[18:19], v[34:35]
	v_pk_add_f32 v[14:15], v[14:15], v[26:27]
	v_pk_add_f32 v[76:77], v[16:17], v[76:77]
	v_pk_add_f32 v[60:61], v[16:17], v[60:61]
	v_pk_mul_f32 v[52:53], v[42:43], s[2:3] op_sel_hi:[1,0]
	v_pk_mul_f32 v[42:43], v[44:45], s[2:3] op_sel_hi:[1,0]
	v_pk_add_f32 v[44:45], v[16:17], v[48:49]
	s_lshl_b64 s[28:29], s[28:29], 12
	global_store_dwordx4 v[30:31], v[38:41], off
	v_lshl_add_u64 v[30:31], v[110:111], 0, v[108:109]
	v_pk_mul_f32 v[20:21], v[20:21], s[2:3] op_sel_hi:[1,0]
	v_pk_mul_f32 v[18:19], v[18:19], s[2:3] op_sel_hi:[1,0]
	v_pk_add_f32 v[16:17], v[16:17], v[28:29]
	v_pk_mul_f32 v[14:15], v[14:15], s[2:3] op_sel_hi:[1,0]
	v_pk_add_f32 v[12:13], v[12:13], v[24:25]
	v_pk_add_f32 v[10:11], v[10:11], v[22:23]
	v_pk_add_f32 v[4:5], v[8:9], v[4:5]
	v_pk_add_f32 v[2:3], v[6:7], v[2:3]
	v_pk_mul_f32 v[76:77], v[76:77], s[2:3] op_sel_hi:[1,0]
	v_pk_mul_f32 v[60:61], v[60:61], s[2:3] op_sel_hi:[1,0]
	v_pk_mul_f32 v[48:49], v[44:45], s[2:3] op_sel_hi:[1,0]
	v_pk_mul_f32 v[44:45], v[46:47], s[2:3] op_sel_hi:[1,0]
	v_lshl_add_u64 v[46:47], v[50:51], 0, s[28:29]
	v_cvt_pk_f16_f32 v18, v18, v19
	v_cvt_pk_f16_f32 v19, v20, v21
	v_pk_mul_f32 v[16:17], v[16:17], s[2:3] op_sel_hi:[1,0]
	v_cvt_pk_f16_f32 v20, v14, v15
	v_lshl_add_u64 v[14:15], v[30:31], 0, s[28:29]
	v_pk_mul_f32 v[12:13], v[12:13], s[2:3] op_sel_hi:[1,0]
	v_pk_mul_f32 v[10:11], v[10:11], s[2:3] op_sel_hi:[1,0]
	v_pk_mul_f32 v[4:5], v[4:5], s[2:3] op_sel_hi:[1,0]
	v_pk_mul_f32 v[2:3], v[2:3], s[2:3] op_sel_hi:[1,0]
	s_add_u32 s28, s20, s22
	v_cvt_pk_f16_f32 v81, v76, v77
	v_cvt_pk_f16_f32 v62, v62, v63
	v_cvt_pk_f16_f32 v63, v66, v67
	v_cvt_pk_f16_f32 v65, v60, v61
	v_cvt_pk_f16_f32 v42, v42, v43
	v_cvt_pk_f16_f32 v43, v52, v53
	v_cvt_pk_f16_f32 v44, v44, v45
	v_cvt_pk_f16_f32 v45, v48, v49
	v_cvt_pk_f16_f32 v21, v16, v17
	v_cvt_pk_f16_f32 v10, v10, v11
	v_cvt_pk_f16_f32 v11, v12, v13
	v_cvt_pk_f16_f32 v12, v2, v3
	v_cvt_pk_f16_f32 v13, v4, v5
	v_lshl_add_u64 v[2:3], v[30:31], 0, s[14:15]
	s_addc_u32 s29, s21, 0
	v_lshlrev_b32_e32 v92, 2, v1
	global_store_dwordx4 v[74:75], v[78:81], off
	global_store_dwordx4 v[58:59], v[62:65], off
	global_store_dwordx4 v[46:47], v[42:45], off
	global_store_dwordx4 v[14:15], v[18:21], off
	global_store_dwordx4 v[2:3], v[10:13], off
	v_lshl_add_u64 v[2:3], s[28:29], 0, v[92:93]
	s_mov_b64 s[28:29], 0x1000
	v_lshl_add_u64 v[10:11], v[2:3], 0, s[28:29]
	global_load_dwordx4 v[22:25], v[10:11], off
	global_load_dwordx4 v[14:17], v[10:11], off offset:16
	global_load_dwordx4 v[6:9], v[10:11], off offset:512
	global_load_dwordx4 v[2:5], v[10:11], off offset:528
	s_mov_b32 s25, 1
	s_mov_b32 s26, 16
	s_mov_b32 s14, 2
	s_mov_b32 s15, 0x18000
	s_mov_b32 s2, 0xc000
	s_mov_b32 s27, 0
	v_mov_b32_e32 v10, v93
	v_mov_b32_e32 v11, v93
	v_mov_b32_e32 v12, v93
	v_mov_b32_e32 v13, v93
	v_mov_b32_e32 v18, v93
	v_mov_b32_e32 v19, v93
	v_mov_b32_e32 v20, v93
	v_mov_b32_e32 v21, v93
	v_mov_b32_e32 v26, v93
	v_mov_b32_e32 v27, v93
	v_mov_b32_e32 v28, v93
	v_mov_b32_e32 v29, v93
	v_mov_b32_e32 v34, v93
	v_mov_b32_e32 v35, v93
	v_mov_b32_e32 v36, v93
	v_mov_b32_e32 v37, v93
	v_mov_b32_e32 v42, v93
	v_mov_b32_e32 v43, v93
	v_mov_b32_e32 v44, v93
	v_mov_b32_e32 v45, v93
	v_mov_b32_e32 v50, v93
	v_mov_b32_e32 v51, v93
	v_mov_b32_e32 v52, v93
	v_mov_b32_e32 v53, v93
	v_mov_b32_e32 v62, v93
	v_mov_b32_e32 v63, v93
	v_mov_b32_e32 v64, v93
	v_mov_b32_e32 v65, v93
	v_mov_b32_e32 v70, v93
	v_mov_b32_e32 v71, v93
	v_mov_b32_e32 v72, v93
	v_mov_b32_e32 v73, v93
	v_mov_b32_e32 v30, v93
	v_mov_b32_e32 v31, v93
	v_mov_b32_e32 v32, v93
	v_mov_b32_e32 v33, v93
	v_mov_b32_e32 v38, v93
	v_mov_b32_e32 v39, v93
	v_mov_b32_e32 v40, v93
	v_mov_b32_e32 v41, v93
	v_mov_b32_e32 v46, v93
	v_mov_b32_e32 v47, v93
	v_mov_b32_e32 v48, v93
	v_mov_b32_e32 v49, v93
	v_mov_b32_e32 v54, v93
	v_mov_b32_e32 v55, v93
	v_mov_b32_e32 v56, v93
	v_mov_b32_e32 v57, v93
	v_mov_b32_e32 v58, v93
	v_mov_b32_e32 v59, v93
	v_mov_b32_e32 v60, v93
	v_mov_b32_e32 v61, v93
	v_mov_b32_e32 v66, v93
	v_mov_b32_e32 v67, v93
	v_mov_b32_e32 v68, v93
	v_mov_b32_e32 v69, v93
	v_mov_b32_e32 v74, v93
	v_mov_b32_e32 v75, v93
	v_mov_b32_e32 v76, v93
	v_mov_b32_e32 v77, v93
	v_mov_b32_e32 v78, v93
	v_mov_b32_e32 v79, v93
	v_mov_b32_e32 v80, v93
	v_mov_b32_e32 v81, v93
.LBB1_5:
	s_mov_b32 s28, s2
	v_add_u32_e32 v1, s28, v101
	ds_read_b128 v[106:109], v1 offset:16384
	ds_read_b128 v[110:113], v1 offset:17408
	ds_read_b128 v[114:117], v1 offset:18432
	ds_read_b128 v[118:121], v1 offset:19456
	ds_read_b128 v[122:125], v1 offset:32768
	ds_read_b128 v[126:129], v1 offset:33792
	ds_read_b128 v[130:133], v1 offset:34816
	ds_read_b128 v[134:137], v1 offset:35840
	v_add_u32_e32 v1, s28, v91
	ds_read_b128 v[138:141], v1
	ds_read_b128 v[142:145], v1 offset:1024
	ds_read_b128 v[146:149], v1 offset:2048
	ds_read_b128 v[150:153], v1 offset:3072
	ds_read_b128 v[154:157], v1 offset:4096
	ds_read_b128 v[158:161], v1 offset:5120
	ds_read_b128 v[162:165], v1 offset:6144
	ds_read_b128 v[166:169], v1 offset:7168
	s_lshl_b32 s2, s25, 2
	s_or_b32 s2, s2, s23
	s_lshl_b64 s[30:31], s[2:3], 19
	s_add_u32 s2, s6, s30
	s_addc_u32 s29, s7, s31
	s_lshl_b32 s33, s14, 7
	s_ashr_i32 s35, s33, 31
	s_add_u32 s30, s2, s33
	s_addc_u32 s31, s29, s35
	s_add_u32 s34, s4, s33
	s_addc_u32 s35, s5, s35
	s_add_i32 s2, s19, s27
	s_add_i32 m0, s2, 0x4000
	s_nop 0
	global_load_lds_dwordx4 v84, s[30:31]
	s_add_i32 m0, s2, 0x6000
	s_nop 0
	global_load_lds_dwordx4 v88, s[30:31]
	s_mov_b32 m0, s2
	s_nop 0
	global_load_lds_dwordx4 v82, s[34:35]
	s_waitcnt vmcnt(3)
	s_waitcnt lgkmcnt(0)
	s_barrier
	s_setprio 1
	s_waitcnt lgkmcnt(0)
	v_mfma_f32_16x16x32_f16 v[78:81], v[106:109], v[138:141], v[78:81]
	s_add_u32 s30, s30, 0x40000
	s_addc_u32 s31, s31, 0
	s_add_i32 m0, s2, 0x8000
	v_mfma_f32_16x16x32_f16 v[74:77], v[114:117], v[138:141], v[74:77]
	global_load_lds_dwordx4 v84, s[30:31]
	s_add_i32 m0, s2, 0xa000
	v_mfma_f32_16x16x32_f16 v[66:69], v[106:109], v[146:149], v[66:69]
	global_load_lds_dwordx4 v88, s[30:31]
	s_add_i32 m0, s2, 0x2000
	v_mfma_f32_16x16x32_f16 v[58:61], v[114:117], v[146:149], v[58:61]
	global_load_lds_dwordx4 v86, s[34:35]
	v_mfma_f32_16x16x32_f16 v[78:81], v[110:113], v[142:145], v[78:81]
	v_mfma_f32_16x16x32_f16 v[74:77], v[118:121], v[142:145], v[74:77]
	v_mfma_f32_16x16x32_f16 v[66:69], v[110:113], v[150:153], v[66:69]
	v_mfma_f32_16x16x32_f16 v[58:61], v[118:121], v[150:153], v[58:61]
	v_mfma_f32_16x16x32_f16 v[54:57], v[106:109], v[154:157], v[54:57]
	v_mfma_f32_16x16x32_f16 v[46:49], v[114:117], v[154:157], v[46:49]
	v_mfma_f32_16x16x32_f16 v[38:41], v[106:109], v[162:165], v[38:41]
	v_mfma_f32_16x16x32_f16 v[30:33], v[114:117], v[162:165], v[30:33]
	v_mfma_f32_16x16x32_f16 v[54:57], v[110:113], v[158:161], v[54:57]
	v_mfma_f32_16x16x32_f16 v[46:49], v[118:121], v[158:161], v[46:49]
	v_mfma_f32_16x16x32_f16 v[38:41], v[110:113], v[166:169], v[38:41]
	v_mfma_f32_16x16x32_f16 v[30:33], v[118:121], v[166:169], v[30:33]
	v_mfma_f32_16x16x32_f16 v[70:73], v[122:125], v[138:141], v[70:73]
	v_mfma_f32_16x16x32_f16 v[62:65], v[130:133], v[138:141], v[62:65]
	v_mfma_f32_16x16x32_f16 v[50:53], v[122:125], v[146:149], v[50:53]
	v_mfma_f32_16x16x32_f16 v[42:45], v[130:133], v[146:149], v[42:45]
	v_mfma_f32_16x16x32_f16 v[70:73], v[126:129], v[142:145], v[70:73]
	v_mfma_f32_16x16x32_f16 v[62:65], v[134:137], v[142:145], v[62:65]
	v_mfma_f32_16x16x32_f16 v[50:53], v[126:129], v[150:153], v[50:53]
	v_mfma_f32_16x16x32_f16 v[42:45], v[134:137], v[150:153], v[42:45]
	v_mfma_f32_16x16x32_f16 v[34:37], v[122:125], v[154:157], v[34:37]
	v_mfma_f32_16x16x32_f16 v[26:29], v[130:133], v[154:157], v[26:29]
	s_add_i32 s14, s14, 1
	s_bitcmp1_b32 s14, 4
	s_addc_u32 s25, s25, 0
	v_mfma_f32_16x16x32_f16 v[18:21], v[122:125], v[162:165], v[18:21]
	s_and_b32 s14, s14, 15
	v_mfma_f32_16x16x32_f16 v[10:13], v[130:133], v[162:165], v[10:13]
	v_mfma_f32_16x16x32_f16 v[34:37], v[126:129], v[158:161], v[34:37]
	v_mfma_f32_16x16x32_f16 v[26:29], v[134:137], v[158:161], v[26:29]
	s_add_i32 s26, s26, -1
	v_mfma_f32_16x16x32_f16 v[18:21], v[126:129], v[166:169], v[18:21]
	s_mov_b32 s2, s15
	s_mov_b32 s15, s27
	v_mfma_f32_16x16x32_f16 v[10:13], v[134:137], v[166:169], v[10:13]
	s_mov_b32 s27, s28
	s_cmp_lg_u32 s26, 0
	s_setprio 0
	s_barrier
	s_cbranch_scc1 .LBB1_5
	s_ashr_i32 s2, s17, 7
	s_and_b32 s3, s2, -16
	s_or_b32 s2, s3, 2
	s_sub_u32 s14, s10, s8
	s_subb_u32 s11, s11, s9
	s_bfe_u32 s6, s17, 0x50006
	s_add_u32 s14, s8, s14
	s_addc_u32 s15, s9, s11
	s_lshr_b32 s11, s24, 6
	s_or_b32 s17, s11, s3
	s_lshl_b32 s17, s17, 8
	s_lshl_b32 s23, s6, 3
	v_bfe_u32 v93, v105, 3, 3
	v_pk_add_f32 v[80:81], v[24:25], v[80:81]
	v_pk_add_f32 v[78:79], v[22:23], v[78:79]
	v_pk_add_f32 v[74:75], v[14:15], v[74:75]
	s_or_b32 s17, s17, s23
	s_or_b32 s11, s2, s11
	v_cvt_pk_f16_f32 v78, v78, v79
	v_cvt_pk_f16_f32 v79, v80, v81
	v_cvt_pk_f16_f32 v80, v74, v75
	v_or_b32_e32 v74, s17, v93
	s_lshl_b32 s11, s11, 8
	v_ashrrev_i32_e32 v75, 31, v74
	v_pk_add_f32 v[72:73], v[8:9], v[72:73]
	v_pk_add_f32 v[70:71], v[6:7], v[70:71]
	v_pk_add_f32 v[62:63], v[2:3], v[62:63]
	s_or_b32 s11, s11, s23
	v_lshlrev_b64 v[74:75], 10, v[74:75]
	v_cvt_pk_f16_f32 v70, v70, v71
	v_cvt_pk_f16_f32 v71, v72, v73
	v_cvt_pk_f16_f32 v72, v62, v63
	v_or_b32_e32 v62, s11, v93
	v_pk_add_f32 v[76:77], v[16:17], v[76:77]
	v_lshl_add_u64 v[74:75], s[14:15], 0, v[74:75]
	v_ashrrev_i32_e32 v63, 31, v62
	v_cvt_pk_f16_f32 v81, v76, v77
	v_lshl_add_u64 v[76:77], v[74:75], 0, v[98:99]
	v_lshlrev_b64 v[62:63], 10, v[62:63]
	global_store_dwordx4 v[76:77], v[78:81], off
	v_pk_add_f32 v[64:65], v[4:5], v[64:65]
	v_lshl_add_u64 v[76:77], s[14:15], 0, v[62:63]
	v_cvt_pk_f16_f32 v73, v64, v65
	v_lshl_add_u64 v[62:63], v[76:77], 0, v[98:99]
	global_store_dwordx4 v[62:63], v[70:73], off
	v_pk_add_f32 v[64:65], v[24:25], v[68:69]
	v_pk_add_f32 v[62:63], v[22:23], v[66:67]
	v_pk_add_f32 v[60:61], v[16:17], v[60:61]
	v_pk_add_f32 v[58:59], v[14:15], v[58:59]
	v_pk_add_f32 v[52:53], v[8:9], v[52:53]
	v_pk_add_f32 v[50:51], v[6:7], v[50:51]
	v_pk_add_f32 v[44:45], v[4:5], v[44:45]
	v_pk_add_f32 v[42:43], v[2:3], v[42:43]
	v_cvt_pk_f16_f32 v62, v62, v63
	v_cvt_pk_f16_f32 v63, v64, v65
	v_cvt_pk_f16_f32 v64, v58, v59
	v_cvt_pk_f16_f32 v65, v60, v61
	v_lshl_add_u64 v[58:59], v[74:75], 0, v[96:97]
	v_cvt_pk_f16_f32 v50, v50, v51
	v_cvt_pk_f16_f32 v51, v52, v53
	v_cvt_pk_f16_f32 v52, v42, v43
	v_cvt_pk_f16_f32 v53, v44, v45
	v_lshl_add_u64 v[42:43], v[76:77], 0, v[96:97]
	v_mov_b32_e32 v1, 0
	global_store_dwordx4 v[58:59], v[62:65], off
	global_store_dwordx4 v[42:43], v[50:53], off
	v_pk_add_f32 v[44:45], v[24:25], v[56:57]
	v_pk_add_f32 v[42:43], v[22:23], v[54:55]
	v_mov_b32_e32 v95, v1
	v_cvt_pk_f16_f32 v42, v42, v43
	v_cvt_pk_f16_f32 v43, v44, v45
	v_pk_add_f32 v[48:49], v[16:17], v[48:49]
	v_pk_add_f32 v[44:45], v[14:15], v[46:47]
	v_pk_add_f32 v[36:37], v[8:9], v[36:37]
	v_pk_add_f32 v[34:35], v[6:7], v[34:35]
	v_pk_add_f32 v[28:29], v[4:5], v[28:29]
	v_pk_add_f32 v[26:27], v[2:3], v[26:27]
	v_pk_add_f32 v[24:25], v[24:25], v[40:41]
	v_pk_add_f32 v[22:23], v[22:23], v[38:39]
	v_pk_add_f32 v[16:17], v[16:17], v[32:33]
	v_pk_add_f32 v[14:15], v[14:15], v[30:31]
	v_pk_add_f32 v[8:9], v[8:9], v[20:21]
	v_pk_add_f32 v[6:7], v[6:7], v[18:19]
	v_pk_add_f32 v[4:5], v[4:5], v[12:13]
	v_pk_add_f32 v[2:3], v[2:3], v[10:11]
	s_add_u32 s14, s20, s22
	v_cvt_pk_f16_f32 v44, v44, v45
	v_cvt_pk_f16_f32 v45, v48, v49
	v_lshl_add_u64 v[46:47], v[74:75], 0, v[0:1]
	v_cvt_pk_f16_f32 v34, v34, v35
	v_cvt_pk_f16_f32 v35, v36, v37
	v_cvt_pk_f16_f32 v36, v26, v27
	v_cvt_pk_f16_f32 v37, v28, v29
	v_lshl_add_u64 v[26:27], v[76:77], 0, v[0:1]
	v_cvt_pk_f16_f32 v22, v22, v23
	v_cvt_pk_f16_f32 v23, v24, v25
	v_cvt_pk_f16_f32 v24, v14, v15
	v_cvt_pk_f16_f32 v25, v16, v17
	v_lshl_add_u64 v[14:15], v[74:75], 0, v[94:95]
	v_cvt_pk_f16_f32 v6, v6, v7
	v_cvt_pk_f16_f32 v7, v8, v9
	v_cvt_pk_f16_f32 v8, v2, v3
	v_cvt_pk_f16_f32 v9, v4, v5
	v_lshl_add_u64 v[2:3], v[76:77], 0, v[94:95]
	s_addc_u32 s15, s21, 0
	v_mov_b32_e32 v93, v1
	global_store_dwordx4 v[46:47], v[42:45], off
	global_store_dwordx4 v[26:27], v[34:37], off
	global_store_dwordx4 v[14:15], v[22:25], off
	global_store_dwordx4 v[2:3], v[6:9], off
	v_lshl_add_u64 v[2:3], s[14:15], 0, v[92:93]
	s_mov_b64 s[14:15], 0x2000
	v_lshl_add_u64 v[2:3], v[2:3], 0, s[14:15]
	global_load_dwordx4 v[20:23], v[2:3], off
	global_load_dwordx4 v[12:15], v[2:3], off offset:16
	global_load_dwordx4 v[8:11], v[2:3], off offset:512
	global_load_dwordx4 v[4:7], v[2:3], off offset:528
	s_add_u32 s11, s12, 0x400000
	s_mov_b32 s7, 2
	v_and_b32_e32 v106, 56, v105
	s_mov_b32 s10, 0
	s_addc_u32 s12, s13, 0
	s_mov_b32 s14, 0xc000
	s_mov_b32 s17, 0x18000
	s_mov_b32 s13, 16
	v_mov_b32_e32 v0, v1
	v_mov_b32_e32 v2, v1
	v_mov_b32_e32 v3, v1
	v_mov_b32_e32 v16, v1
	v_mov_b32_e32 v17, v1
	v_mov_b32_e32 v18, v1
	v_mov_b32_e32 v19, v1
	v_mov_b32_e32 v24, v1
	v_mov_b32_e32 v25, v1
	v_mov_b32_e32 v26, v1
	v_mov_b32_e32 v27, v1
	v_mov_b32_e32 v32, v1
	v_mov_b32_e32 v33, v1
	v_mov_b32_e32 v34, v1
	v_mov_b32_e32 v35, v1
	v_mov_b32_e32 v40, v1
	v_mov_b32_e32 v41, v1
	v_mov_b32_e32 v42, v1
	v_mov_b32_e32 v43, v1
	v_mov_b32_e32 v48, v1
	v_mov_b32_e32 v49, v1
	v_mov_b32_e32 v50, v1
	v_mov_b32_e32 v51, v1
	v_mov_b32_e32 v60, v1
	v_mov_b32_e32 v61, v1
	v_mov_b32_e32 v62, v1
	v_mov_b32_e32 v63, v1
	v_mov_b32_e32 v68, v1
	v_mov_b32_e32 v69, v1
	v_mov_b32_e32 v70, v1
	v_mov_b32_e32 v71, v1
	v_mov_b32_e32 v28, v1
	v_mov_b32_e32 v29, v1
	v_mov_b32_e32 v30, v1
	v_mov_b32_e32 v31, v1
	v_mov_b32_e32 v36, v1
	v_mov_b32_e32 v37, v1
	v_mov_b32_e32 v38, v1
	v_mov_b32_e32 v39, v1
	v_mov_b32_e32 v44, v1
	v_mov_b32_e32 v45, v1
	v_mov_b32_e32 v46, v1
	v_mov_b32_e32 v47, v1
	v_mov_b32_e32 v52, v1
	v_mov_b32_e32 v53, v1
	v_mov_b32_e32 v54, v1
	v_mov_b32_e32 v55, v1
	v_mov_b32_e32 v56, v1
	v_mov_b32_e32 v57, v1
	v_mov_b32_e32 v58, v1
	v_mov_b32_e32 v59, v1
	v_mov_b32_e32 v64, v1
	v_mov_b32_e32 v65, v1
	v_mov_b32_e32 v66, v1
	v_mov_b32_e32 v67, v1
	v_mov_b32_e32 v72, v1
	v_mov_b32_e32 v73, v1
	v_mov_b32_e32 v74, v1
	v_mov_b32_e32 v75, v1
	v_mov_b32_e32 v76, v1
	v_mov_b32_e32 v77, v1
	v_mov_b32_e32 v78, v1
	v_mov_b32_e32 v79, v1
